# in-proj K-loop: first iteration after an epilogue waits vmcnt(24) in phase 4 (older DMAs only) and vmcnt(10) in phase 6, so the K-loop restart no longer waits for the 16 epilogue stores; plus previous
# speedup vs baseline: 1.0046x; 1.0011x over previous
; template <bool PERM, class Epi, class Sched>
; __device__ __forceinline__ void gemm_phase(LAS unsigned char* lds, const Sched& S, const Epi& E) {
;     ...
;     GUnit cur, nxt; int ui = 0;
;     if (!S.next(0, cur)) return;
;     __device__ __forceinline__ bool next(int i, gm::GUnit& u) const {
;         const int L = i * G + c, nlat = 256 * 16, nproj = nlat + (l == 0 ? 8 * 16 : 8 * 4), ngate = (l == 0 ? 264 : 256) * 16;
;         if (L >= nproj + ngate) return false;
;         int pm, pn, sub = 0;
;         if (L < nlat) grouped_order(L, 256, 16, pm, pn);
;         else if (L < nproj) { const int r = L - nlat; if (l == 0) { pm = 256 + (r >> 4); pn = r & 15; } else { pm = 256 + (r >> 2); pn = 2 + (r & 3); } }
;         else { grouped_order(L - nproj, l == 0 ? 264 : 256, 16, pm, pn); sub = 1; }
.LBB0_225:
	v_writelane_b32 v255, s54, 11
	s_andn2_b64 vcc, exec, s[8:9]
	s_nop 0
	v_writelane_b32 v255, s55, 12
	s_cbranch_vccnz .LBB0_318
	s_mov_b32 s100, 0
	s_and_b64 s[0:1], s[64:65], exec
	s_movk_i32 s0, 0x2100
	v_mov_b32_e32 v1, v0
	s_cselect_b32 s31, s0, 0x2020
	v_readlane_b32 s0, v254, 62
	s_cmp_ge_i32 s0, s31
	v_readfirstlane_b32 s30, v1
	v_readlane_b32 s1, v254, 63
	s_cbranch_scc1 .LBB0_268
	s_add_u32 s8, s56, 0x916100
	s_addc_u32 s9, s57, 0
	s_and_b64 s[0:1], s[64:65], exec
	s_movk_i32 s0, 0x1080
	s_cselect_b32 s58, s0, 0x1020
	v_readlane_b32 s0, v252, 44
	v_readlane_b32 s1, v252, 45
	s_andn2_b64 vcc, exec, s[0:1]
	s_mov_b32 s0, 0
	s_cbranch_vccnz .LBB0_233
	v_readlane_b32 s0, v254, 62
	s_cmp_ge_u32 s0, s58
	s_mov_b64 s[22:23], -1
	v_readlane_b32 s1, v254, 63
	s_cbranch_scc0 .LBB0_230
	s_add_u32 s18, s56, 0x1916100
	v_readlane_b32 s0, v254, 62
	s_addc_u32 s19, s57, 0
	v_readlane_b32 s1, v254, 63
	s_sub_i32 s2, s0, s58
	s_and_b64 s[0:1], s[64:65], exec
	s_movk_i32 s0, 0x108
	s_cselect_b32 s0, s0, 0x100
	v_readlane_b32 s1, v252, 46
	s_mul_i32 s1, s0, s1
	s_lshr_b32 s2, s2, 3
	s_add_i32 s2, s2, s1
	s_lshr_b32 s1, s2, 4
	s_and_b32 s7, s1, 0x1fffff8
	s_sub_i32 s0, s0, s7
	s_min_i32 s22, s0, 8
	s_sext_i32_i8 s0, s22
	s_waitcnt vmcnt(0)
	v_cvt_f32_i32_e32 v2, s0
	s_and_b32 s2, s2, 0x7f
	v_cvt_f32_ubyte0_e32 v4, s2
	s_ashr_i32 s0, s0, 30
	v_rcp_iflag_f32_e32 v3, v2
	s_or_b32 s23, s0, 1
	v_mul_f32_e32 v3, v4, v3
	v_trunc_f32_e32 v3, v3
	v_fma_f32 v4, -v3, v2, v4
	v_cvt_i32_f32_e32 v3, v3
	v_cmp_ge_f32_e64 s[0:1], |v4|, |v2|
	s_and_b64 s[0:1], s[0:1], exec
	s_cselect_b32 s0, s23, 0
	v_readfirstlane_b32 s1, v3
	s_add_i32 s0, s1, s0
	s_sext_i32_i8 s74, s0
	s_mul_i32 s0, s0, s22
	s_sub_i32 s0, s2, s0
	s_and_b32 s0, s0, 0xff
	s_add_i32 s72, s7, s0
	s_mov_b64 s[22:23], 0

; template <bool PERM, class Epi, class Sched>
; __device__ __forceinline__ void gemm_phase(LAS unsigned char* lds, const Sched& S, const Epi& E) {
;     ...
;     for (;;) {
;         const bool has_next = S.next(ui + 1, nxt);
;         const char* nA = cA; const char* nB = cB;
;         if (has_next) { nA = nxt.A; nB = nxt.B; }
;         if (Sched::GATHER_A) {
;             na00 = va00; na01 = va01; na10 = va10; na11 = va11; nb0 = vb0; nb1 = vb1; nhsB = hsB;
;             if (has_next) {
;                 if (nxt.gidx != nullptr && nxt.gidx == cur.gidx) {
;                     unsigned t0, t1, t2, t3; gm::GUnit ub = nxt; ub.gidx = nullptr; G_OFFS(ub, t0, t1, t2, t3, nb0, nb1, nhsB); (void)t0; (void)t1; (void)t2; (void)t3;
;                 } else G_OFFS(nxt, na00, na01, na10, na11, nb0, nb1, nhsB);
;             }
;         }
;         const int nt = cur.nt;
.LBB0_237:
	s_mov_b32 s100, 1
	s_and_b64 vcc, exec, s[52:53]
	s_mov_b32 s72, s66
	s_mov_b32 s74, s54
	s_mov_b32 s0, s91
	s_mov_b64 s[8:9], s[68:69]
	s_mov_b64 s[18:19], s[70:71]
	s_cbranch_vccnz .LBB0_265

; #define G_STAGE2(bufoff, gbase, v0, v1) do { \
;         __builtin_amdgcn_global_load_lds((const unsigned*)((const char*)(gbase) + (v0)), (LAS unsigned*)(lds + (bufoff) + ldsw), 16, 0, 0); \
;         __builtin_amdgcn_global_load_lds((const unsigned*)((const char*)(gbase) + (v1)), (LAS unsigned*)(lds + (bufoff) + ldsw + 8192), 16, 0, 0); } while (0)
; #define G_LDA(dst, b, h) do { _Pragma("unroll") for (int m = 0; m < 4; ++m) _Pragma("unroll") for (int k = 0; k < 2; ++k) dst[m][k] = *(const LAS bf16x8*)(lds + G_SA(b, h) + aoff + m * 2048 + k * 1024); } while (0)
; #define G_LDB(dst, b, h) do { _Pragma("unroll") for (int n = 0; n < 2; ++n) _Pragma("unroll") for (int k = 0; k < 2; ++k) dst[n][k] = *(const LAS bf16x8*)(lds + G_SB(b, h) + boff + n * 2048 + k * 1024); } while (0)
; #define G_WAIT_V(n) asm volatile("s_waitcnt vmcnt(" #n ")" ::: "memory")
; #define G_WAIT_L(n) asm volatile("s_waitcnt lgkmcnt(" #n ")" ::: "memory")
; #define G_BAR __builtin_amdgcn_s_barrier()
; #define G_SCHED __builtin_amdgcn_sched_barrier(0)
; template <bool PERM, class Epi, class Sched>
; __device__ __forceinline__ void gemm_phase(LAS unsigned char* lds, const Sched& S, const Epi& E) {
;     ...
;         for (int t = 0; t < nt; t += 2) {
;             const bool last = (t == nt - 2);
;             const char* a1 = cA + (size_t)(t + 1) * kstep;
;             G_LDB(B0, 0, 0); G_SCHED; G_LDA(At, 0, 0); G_STAGE2(G_SA(1, 1), a1, va10, va11);
;             const char* a2 = last ? nA : cA + (size_t)(t + 2) * kstep; const char* b2 = last ? nB : cB + (size_t)(t + 2) * kstep;
;             if (last) {
;                 if (Sched::GATHER_A) { va00 = na00; va01 = na01; va10 = na10; va11 = na11; vb0 = nb0; vb1 = nb1; hsB = nhsB; }
;                 else if (has_next) G_OFFS(nxt, va00, va01, va10, va11, vb0, vb1, hsB);
;             }
;             const char* a3 = a2 + kstep; const char* b3 = b2 + kstep;
;             G_WAIT_L(8); G_BAR; G_WAIT_L(0); G_MMA(0, 0, At, B0); G_BAR; G_SCHED;
;             G_LDB(B1, 0, 1); G_STAGE2(G_SB(0, 0), b2, vb0, vb1);
;             G_BAR; G_WAIT_L(0); G_MMA(0, 1, At, B1); G_BAR;
;             G_LDA(At, 0, 1); G_STAGE2(G_SA(0, 0), a2, va00, va01);
;             G_BAR; G_WAIT_L(0); G_MMA(1, 0, At, B0); G_BAR; G_SCHED;
;             G_STAGE2(G_SB(0, 1), b2 + hsB, vb0, vb1);
;             G_WAIT_V(6); G_BAR; G_MMA(1, 1, At, B1); G_BAR;
.LBB0_253:
	s_add_u32 s18, s28, 0x80
	s_waitcnt lgkmcnt(8)
	s_barrier
	s_waitcnt lgkmcnt(0)
	s_addc_u32 s19, s29, 0
	s_and_b64 s[8:9], s[8:9], exec
	v_mov_b32_e32 v205, v147
	v_mov_b32_e32 v207, v147
	s_cselect_b32 s19, s69, s19
	s_cselect_b32 s18, s68, s18
	s_cselect_b32 s9, s71, s2
	s_cselect_b32 s8, s70, s1
	s_setprio 1
	s_waitcnt lgkmcnt(0)
	v_mfma_f32_16x16x32_bf16 v[126:129], v[130:133], v[172:175], v[126:129]
	v_mfma_f32_16x16x32_bf16 v[122:125], v[138:141], v[172:175], v[122:125]
	v_mfma_f32_16x16x32_bf16 v[118:121], v[130:133], v[164:167], v[118:121]
	v_mfma_f32_16x16x32_bf16 v[114:117], v[138:141], v[164:167], v[114:117]
	v_mfma_f32_16x16x32_bf16 v[110:113], v[130:133], v[156:159], v[110:113]
	v_mfma_f32_16x16x32_bf16 v[106:109], v[138:141], v[156:159], v[106:109]
	v_mfma_f32_16x16x32_bf16 v[102:105], v[130:133], v[148:151], v[102:105]
	v_mfma_f32_16x16x32_bf16 v[98:101], v[138:141], v[148:151], v[98:101]
	v_mfma_f32_16x16x32_bf16 v[126:129], v[134:137], v[176:179], v[126:129]
	v_mfma_f32_16x16x32_bf16 v[122:125], v[142:145], v[176:179], v[122:125]
	v_mfma_f32_16x16x32_bf16 v[118:121], v[134:137], v[168:171], v[118:121]
	v_mfma_f32_16x16x32_bf16 v[114:117], v[142:145], v[168:171], v[114:117]
	v_mfma_f32_16x16x32_bf16 v[110:113], v[134:137], v[160:163], v[110:113]
	v_mfma_f32_16x16x32_bf16 v[106:109], v[142:145], v[160:163], v[106:109]
	v_mfma_f32_16x16x32_bf16 v[102:105], v[134:137], v[152:155], v[102:105]
	v_mfma_f32_16x16x32_bf16 v[98:101], v[142:145], v[152:155], v[98:101]
	s_setprio 0
	s_barrier
	s_add_i32 s24, 0, 0x14000
	s_mov_b32 m0, s65
	v_add_u32_e32 v192, s24, v1
	ds_read_b128 v[180:183], v192
	ds_read_b128 v[184:187], v192 offset:1024
	ds_read_b128 v[188:191], v192 offset:2048
	ds_read_b128 v[192:195], v192 offset:3072
	global_load_lds_dwordx4 v146, s[8:9]
	s_mov_b32 m0, s73
	v_mov_b32_e32 v209, v147
	global_load_lds_dwordx4 v208, s[8:9]
	s_barrier
	s_waitcnt lgkmcnt(0)
	v_lshl_add_u64 v[210:211], s[8:9], 0, v[146:147]
	v_lshl_add_u64 v[212:213], s[8:9], 0, v[208:209]
	s_setprio 1
	s_waitcnt lgkmcnt(0)
	v_mfma_f32_16x16x32_bf16 v[62:65], v[180:183], v[172:175], v[62:65]
	v_mfma_f32_16x16x32_bf16 v[58:61], v[188:191], v[172:175], v[58:61]
	v_mfma_f32_16x16x32_bf16 v[54:57], v[180:183], v[164:167], v[54:57]
	v_mfma_f32_16x16x32_bf16 v[50:53], v[188:191], v[164:167], v[50:53]
	v_mfma_f32_16x16x32_bf16 v[46:49], v[180:183], v[156:159], v[46:49]
	v_mfma_f32_16x16x32_bf16 v[42:45], v[188:191], v[156:159], v[42:45]
	v_mfma_f32_16x16x32_bf16 v[38:41], v[180:183], v[148:151], v[38:41]
	v_mfma_f32_16x16x32_bf16 v[34:37], v[188:191], v[148:151], v[34:37]
	v_mfma_f32_16x16x32_bf16 v[62:65], v[184:187], v[176:179], v[62:65]
	v_mfma_f32_16x16x32_bf16 v[58:61], v[192:195], v[176:179], v[58:61]
	v_mfma_f32_16x16x32_bf16 v[54:57], v[184:187], v[168:171], v[54:57]
	v_mfma_f32_16x16x32_bf16 v[50:53], v[192:195], v[168:171], v[50:53]
	v_mfma_f32_16x16x32_bf16 v[46:49], v[184:187], v[160:163], v[46:49]
	v_mfma_f32_16x16x32_bf16 v[42:45], v[192:195], v[160:163], v[42:45]
	v_mfma_f32_16x16x32_bf16 v[38:41], v[184:187], v[152:155], v[38:41]
	v_mfma_f32_16x16x32_bf16 v[34:37], v[192:195], v[152:155], v[34:37]
	s_setprio 0
	s_mov_b32 m0, s64
	s_barrier
	ds_read_b128 v[148:151], v199 offset:16384
	ds_read_b128 v[152:155], v199 offset:17408
	ds_read_b128 v[156:159], v199 offset:18432
	ds_read_b128 v[160:163], v199 offset:19456
	ds_read_b128 v[164:167], v199 offset:20480
	ds_read_b128 v[168:171], v199 offset:21504
	ds_read_b128 v[172:175], v199 offset:22528
	ds_read_b128 v[176:179], v199 offset:23552
	global_load_lds_dwordx4 v200, s[18:19]
	s_mov_b32 m0, s75
	v_mov_b32_e32 v201, v147
	global_load_lds_dwordx4 v202, s[18:19]
	s_barrier
	s_waitcnt lgkmcnt(0)
	v_mov_b32_e32 v203, v147
	v_lshl_add_u64 v[214:215], s[18:19], 0, v[200:201]
	v_lshl_add_u64 v[216:217], s[18:19], 0, v[202:203]
	s_setprio 1
	s_waitcnt lgkmcnt(0)
	v_mfma_f32_16x16x32_bf16 v[94:97], v[130:133], v[148:151], v[94:97]
	v_mfma_f32_16x16x32_bf16 v[90:93], v[138:141], v[148:151], v[90:93]
	v_mfma_f32_16x16x32_bf16 v[86:89], v[130:133], v[156:159], v[86:89]
	v_mfma_f32_16x16x32_bf16 v[82:85], v[138:141], v[156:159], v[82:85]
	v_mfma_f32_16x16x32_bf16 v[78:81], v[130:133], v[164:167], v[78:81]
	v_mfma_f32_16x16x32_bf16 v[74:77], v[138:141], v[164:167], v[74:77]
	v_mfma_f32_16x16x32_bf16 v[70:73], v[130:133], v[172:175], v[70:73]
	v_mfma_f32_16x16x32_bf16 v[66:69], v[138:141], v[172:175], v[66:69]
	v_mfma_f32_16x16x32_bf16 v[94:97], v[134:137], v[152:155], v[94:97]
	v_mfma_f32_16x16x32_bf16 v[90:93], v[142:145], v[152:155], v[90:93]
	v_mfma_f32_16x16x32_bf16 v[86:89], v[134:137], v[160:163], v[86:89]
	v_mfma_f32_16x16x32_bf16 v[82:85], v[142:145], v[160:163], v[82:85]
	v_mfma_f32_16x16x32_bf16 v[78:81], v[134:137], v[168:171], v[78:81]
	v_mfma_f32_16x16x32_bf16 v[74:77], v[142:145], v[168:171], v[74:77]
	v_mfma_f32_16x16x32_bf16 v[70:73], v[134:137], v[176:179], v[70:73]
	v_mfma_f32_16x16x32_bf16 v[66:69], v[142:145], v[176:179], v[66:69]
	s_setprio 0
	s_barrier
	s_add_u32 s22, s8, 0x40000
	s_addc_u32 s23, s9, 0
	s_add_i32 s24, s24, s63
	s_mov_b32 m0, s24
	s_nop 0
	global_load_lds_dwordx4 v146, s[22:23]
	s_add_i32 m0, s24, 0x2000
	s_nop 0
	global_load_lds_dwordx4 v208, s[22:23]
	s_cmp_lg_u32 s100, 0
	s_cbranch_scc1 .Lpj_p4s
	s_waitcnt vmcnt(6)
	s_branch .Lpj_p4j
.Lpj_p4s:
	s_waitcnt vmcnt(24)
; #define G_STAGE2(bufoff, gbase, v0, v1) do { \
;         __builtin_amdgcn_global_load_lds((const unsigned*)((const char*)(gbase) + (v0)), (LAS unsigned*)(lds + (bufoff) + ldsw), 16, 0, 0); \
;         __builtin_amdgcn_global_load_lds((const unsigned*)((const char*)(gbase) + (v1)), (LAS unsigned*)(lds + (bufoff) + ldsw + 8192), 16, 0, 0); } while (0)
; #define G_LDA(dst, b, h) do { _Pragma("unroll") for (int m = 0; m < 4; ++m) _Pragma("unroll") for (int k = 0; k < 2; ++k) dst[m][k] = *(const LAS bf16x8*)(lds + G_SA(b, h) + aoff + m * 2048 + k * 1024); } while (0)
; #define G_LDB(dst, b, h) do { _Pragma("unroll") for (int n = 0; n < 2; ++n) _Pragma("unroll") for (int k = 0; k < 2; ++k) dst[n][k] = *(const LAS bf16x8*)(lds + G_SB(b, h) + boff + n * 2048 + k * 1024); } while (0)
; #define G_MMA(ai, bj, At, Bt) do { __builtin_amdgcn_s_setprio(1); _Pragma("unroll") for (int m = 0; m < 4; ++m) _Pragma("unroll") for (int n = 0; n < 2; ++n) _Pragma("unroll") for (int k = 0; k < 2; ++k) \
;         acc[ai][bj][m][n] = __builtin_amdgcn_mfma_f32_16x16x32_bf16(Bt[n][k], At[m][k], acc[ai][bj][m][n], 0, 0, 0); __builtin_amdgcn_s_setprio(0); } while (0)
; #define G_WAIT_V(n) asm volatile("s_waitcnt vmcnt(" #n ")" ::: "memory")
; #define G_WAIT_L(n) asm volatile("s_waitcnt lgkmcnt(" #n ")" ::: "memory")
; #define G_BAR __builtin_amdgcn_s_barrier()
; #define G_SCHED __builtin_amdgcn_sched_barrier(0)
; template <bool PERM, class Epi, class Sched>
; __device__ __forceinline__ void gemm_phase(LAS unsigned char* lds, const Sched& S, const Epi& E) {
;     ...
;             G_WAIT_V(6); G_BAR; G_MMA(1, 1, At, B1); G_BAR;
;             G_LDB(B0, 1, 0); G_SCHED; G_LDA(At, 1, 0); G_STAGE2(G_SA(0, 1), a2, va10, va11);
;             G_WAIT_L(8); G_BAR; G_WAIT_L(0); G_MMA(0, 0, At, B0); G_BAR; G_SCHED;
;             G_LDB(B1, 1, 1); G_STAGE2(G_SB(1, 0), b3, vb0, vb1);
;             G_BAR; G_WAIT_L(0); G_MMA(0, 1, At, B1); G_BAR;
.Lpj_p4j:
	s_barrier
	s_setprio 1
	v_mfma_f32_16x16x32_bf16 v[30:33], v[180:183], v[148:151], v[30:33]
	v_mfma_f32_16x16x32_bf16 v[26:29], v[188:191], v[148:151], v[26:29]
	v_mfma_f32_16x16x32_bf16 v[22:25], v[180:183], v[156:159], v[22:25]
	v_mfma_f32_16x16x32_bf16 v[18:21], v[188:191], v[156:159], v[18:21]
	v_mfma_f32_16x16x32_bf16 v[14:17], v[180:183], v[164:167], v[14:17]
	v_mfma_f32_16x16x32_bf16 v[10:13], v[188:191], v[164:167], v[10:13]
	v_mfma_f32_16x16x32_bf16 v[6:9], v[180:183], v[172:175], v[6:9]
	v_mfma_f32_16x16x32_bf16 v[2:5], v[188:191], v[172:175], v[2:5]
	v_mfma_f32_16x16x32_bf16 v[30:33], v[184:187], v[152:155], v[30:33]
	v_mfma_f32_16x16x32_bf16 v[26:29], v[192:195], v[152:155], v[26:29]
	v_mfma_f32_16x16x32_bf16 v[22:25], v[184:187], v[160:163], v[22:25]
	v_mfma_f32_16x16x32_bf16 v[18:21], v[192:195], v[160:163], v[18:21]
	v_mfma_f32_16x16x32_bf16 v[14:17], v[184:187], v[168:171], v[14:17]
	v_mfma_f32_16x16x32_bf16 v[10:13], v[192:195], v[168:171], v[10:13]
	v_mfma_f32_16x16x32_bf16 v[6:9], v[184:187], v[176:179], v[6:9]
	v_mfma_f32_16x16x32_bf16 v[2:5], v[192:195], v[176:179], v[2:5]
	s_setprio 0
	s_add_i32 s22, 0, 0x18000
	v_add_u32_e32 v142, s22, v1
	s_barrier
	ds_read_b128 v[130:133], v142
	ds_read_b128 v[134:137], v142 offset:1024
	ds_read_b128 v[138:141], v142 offset:2048
	ds_read_b128 v[142:145], v142 offset:3072
	s_mov_b32 m0, s80
	v_lshl_add_u64 v[180:181], s[18:19], 0, v[204:205]
	ds_read_b128 v[148:151], v199 offset:32768
	ds_read_b128 v[152:155], v199 offset:33792
	ds_read_b128 v[156:159], v199 offset:34816
	ds_read_b128 v[160:163], v199 offset:35840
	ds_read_b128 v[164:167], v199 offset:36864
	ds_read_b128 v[168:171], v199 offset:37888
	ds_read_b128 v[172:175], v199 offset:38912
	ds_read_b128 v[176:179], v199 offset:39936
	global_load_lds_dwordx4 v[180:181], off
	v_lshl_add_u64 v[180:181], s[18:19], 0, v[206:207]
	s_mov_b32 m0, s81
	s_nop 0
	global_load_lds_dwordx4 v[180:181], off
	s_waitcnt lgkmcnt(8)
	s_barrier
	s_waitcnt lgkmcnt(0)
	s_setprio 1
	s_waitcnt lgkmcnt(0)
	v_mfma_f32_16x16x32_bf16 v[126:129], v[130:133], v[148:151], v[126:129]
	v_mfma_f32_16x16x32_bf16 v[122:125], v[138:141], v[148:151], v[122:125]
	v_mfma_f32_16x16x32_bf16 v[118:121], v[130:133], v[156:159], v[118:121]
	v_mfma_f32_16x16x32_bf16 v[114:117], v[138:141], v[156:159], v[114:117]
	v_mfma_f32_16x16x32_bf16 v[110:113], v[130:133], v[164:167], v[110:113]
	v_mfma_f32_16x16x32_bf16 v[106:109], v[138:141], v[164:167], v[106:109]
	v_mfma_f32_16x16x32_bf16 v[102:105], v[130:133], v[172:175], v[102:105]
	v_mfma_f32_16x16x32_bf16 v[98:101], v[138:141], v[172:175], v[98:101]
	v_mfma_f32_16x16x32_bf16 v[126:129], v[134:137], v[152:155], v[126:129]
	v_mfma_f32_16x16x32_bf16 v[122:125], v[142:145], v[152:155], v[122:125]
	v_mfma_f32_16x16x32_bf16 v[118:121], v[134:137], v[160:163], v[118:121]
	v_mfma_f32_16x16x32_bf16 v[114:117], v[142:145], v[160:163], v[114:117]
	v_mfma_f32_16x16x32_bf16 v[110:113], v[134:137], v[168:171], v[110:113]
	v_mfma_f32_16x16x32_bf16 v[106:109], v[142:145], v[168:171], v[106:109]
	v_mfma_f32_16x16x32_bf16 v[102:105], v[134:137], v[176:179], v[102:105]
	v_mfma_f32_16x16x32_bf16 v[98:101], v[142:145], v[176:179], v[98:101]
	s_setprio 0
	s_barrier
	s_add_i32 s18, 0, 0x1c000
	s_add_i32 s19, s22, s63
	v_add_u32_e32 v192, s18, v1
	v_lshl_add_u64 v[210:211], v[210:211], 0, s[34:35]
	s_mov_b32 m0, s19
	ds_read_b128 v[180:183], v192
	ds_read_b128 v[184:187], v192 offset:1024
	ds_read_b128 v[188:191], v192 offset:2048
	ds_read_b128 v[192:195], v192 offset:3072
	global_load_lds_dwordx4 v[210:211], off
	v_lshl_add_u64 v[210:211], v[212:213], 0, s[34:35]
	s_add_i32 m0, s19, 0x2000
	s_nop 0
	global_load_lds_dwordx4 v[210:211], off
	s_cmp_eq_u32 s100, 0
	s_cbranch_scc1 .Lpj_p6n
	s_waitcnt vmcnt(10)
; #define G_STAGE2(bufoff, gbase, v0, v1) do { \
;         __builtin_amdgcn_global_load_lds((const unsigned*)((const char*)(gbase) + (v0)), (LAS unsigned*)(lds + (bufoff) + ldsw), 16, 0, 0); \
;         __builtin_amdgcn_global_load_lds((const unsigned*)((const char*)(gbase) + (v1)), (LAS unsigned*)(lds + (bufoff) + ldsw + 8192), 16, 0, 0); } while (0)
; #define G_LDA(dst, b, h) do { _Pragma("unroll") for (int m = 0; m < 4; ++m) _Pragma("unroll") for (int k = 0; k < 2; ++k) dst[m][k] = *(const LAS bf16x8*)(lds + G_SA(b, h) + aoff + m * 2048 + k * 1024); } while (0)
; #define G_MMA(ai, bj, At, Bt) do { __builtin_amdgcn_s_setprio(1); _Pragma("unroll") for (int m = 0; m < 4; ++m) _Pragma("unroll") for (int n = 0; n < 2; ++n) _Pragma("unroll") for (int k = 0; k < 2; ++k) \
;         acc[ai][bj][m][n] = __builtin_amdgcn_mfma_f32_16x16x32_bf16(Bt[n][k], At[m][k], acc[ai][bj][m][n], 0, 0, 0); __builtin_amdgcn_s_setprio(0); } while (0)
; #define G_WAIT_V(n) asm volatile("s_waitcnt vmcnt(" #n ")" ::: "memory")
; #define G_WAIT_L(n) asm volatile("s_waitcnt lgkmcnt(" #n ")" ::: "memory")
; #define G_BAR __builtin_amdgcn_s_barrier()
; #define G_SCHED __builtin_amdgcn_sched_barrier(0)
; template <bool PERM, class Epi, class Sched>
; __device__ __forceinline__ void gemm_phase(LAS unsigned char* lds, const Sched& S, const Epi& E) {
;     ...
;             G_BAR; G_WAIT_L(0); G_MMA(0, 1, At, B1); G_BAR;
;             G_LDA(At, 1, 1); G_STAGE2(G_SA(1, 0), a3, va00, va01);
;             G_BAR; G_WAIT_L(0); G_MMA(1, 0, At, B0); G_BAR; G_SCHED;
;             G_STAGE2(G_SB(1, 1), b3 + hsB, vb0, vb1);
;             G_WAIT_V(6); G_BAR; G_MMA(1, 1, At, B1); G_BAR;
;         }
.Lpj_p6n:
	s_barrier
	s_waitcnt lgkmcnt(0)
	s_setprio 1
	s_waitcnt lgkmcnt(0)
	v_mfma_f32_16x16x32_bf16 v[62:65], v[180:183], v[148:151], v[62:65]
	v_mfma_f32_16x16x32_bf16 v[58:61], v[188:191], v[148:151], v[58:61]
	v_mfma_f32_16x16x32_bf16 v[54:57], v[180:183], v[156:159], v[54:57]
	v_mfma_f32_16x16x32_bf16 v[50:53], v[188:191], v[156:159], v[50:53]
	v_mfma_f32_16x16x32_bf16 v[46:49], v[180:183], v[164:167], v[46:49]
	v_mfma_f32_16x16x32_bf16 v[42:45], v[188:191], v[164:167], v[42:45]
	v_mfma_f32_16x16x32_bf16 v[38:41], v[180:183], v[172:175], v[38:41]
	v_mfma_f32_16x16x32_bf16 v[34:37], v[188:191], v[172:175], v[34:37]
	v_mfma_f32_16x16x32_bf16 v[62:65], v[184:187], v[152:155], v[62:65]
	v_mfma_f32_16x16x32_bf16 v[58:61], v[192:195], v[152:155], v[58:61]
	v_mfma_f32_16x16x32_bf16 v[54:57], v[184:187], v[160:163], v[54:57]
	v_mfma_f32_16x16x32_bf16 v[50:53], v[192:195], v[160:163], v[50:53]
	v_mfma_f32_16x16x32_bf16 v[46:49], v[184:187], v[168:171], v[46:49]
	v_mfma_f32_16x16x32_bf16 v[42:45], v[192:195], v[168:171], v[42:45]
	v_mfma_f32_16x16x32_bf16 v[38:41], v[184:187], v[176:179], v[38:41]
	v_mfma_f32_16x16x32_bf16 v[34:37], v[192:195], v[176:179], v[34:37]
	s_setprio 0
	s_mov_b32 m0, s83
	v_lshl_add_u64 v[210:211], v[214:215], 0, s[34:35]
	s_barrier
	ds_read_b128 v[148:151], v199 offset:49152
	ds_read_b128 v[152:155], v199 offset:50176
	ds_read_b128 v[156:159], v199 offset:51200
	ds_read_b128 v[160:163], v199 offset:52224
	ds_read_b128 v[164:167], v199 offset:53248
	ds_read_b128 v[168:171], v199 offset:54272
	ds_read_b128 v[172:175], v199 offset:55296
	ds_read_b128 v[176:179], v199 offset:56320
	global_load_lds_dwordx4 v[210:211], off
	v_lshl_add_u64 v[210:211], v[216:217], 0, s[34:35]
	s_mov_b32 m0, s84
	s_nop 0
	global_load_lds_dwordx4 v[210:211], off
	s_barrier
	s_waitcnt lgkmcnt(0)
	s_setprio 1
	s_waitcnt lgkmcnt(0)
	v_mfma_f32_16x16x32_bf16 v[94:97], v[130:133], v[148:151], v[94:97]
	v_mfma_f32_16x16x32_bf16 v[90:93], v[138:141], v[148:151], v[90:93]
	v_mfma_f32_16x16x32_bf16 v[86:89], v[130:133], v[156:159], v[86:89]
	v_mfma_f32_16x16x32_bf16 v[82:85], v[138:141], v[156:159], v[82:85]
	v_mfma_f32_16x16x32_bf16 v[78:81], v[130:133], v[164:167], v[78:81]
	v_mfma_f32_16x16x32_bf16 v[74:77], v[138:141], v[164:167], v[74:77]
	v_mfma_f32_16x16x32_bf16 v[70:73], v[130:133], v[172:175], v[70:73]
	v_mfma_f32_16x16x32_bf16 v[66:69], v[138:141], v[172:175], v[66:69]
	v_mfma_f32_16x16x32_bf16 v[94:97], v[134:137], v[152:155], v[94:97]
	v_mfma_f32_16x16x32_bf16 v[90:93], v[142:145], v[152:155], v[90:93]
	v_mfma_f32_16x16x32_bf16 v[86:89], v[134:137], v[160:163], v[86:89]
	v_mfma_f32_16x16x32_bf16 v[82:85], v[142:145], v[160:163], v[82:85]
	v_mfma_f32_16x16x32_bf16 v[78:81], v[134:137], v[168:171], v[78:81]
	v_mfma_f32_16x16x32_bf16 v[74:77], v[142:145], v[168:171], v[74:77]
	v_mfma_f32_16x16x32_bf16 v[70:73], v[134:137], v[176:179], v[70:73]
	v_mfma_f32_16x16x32_bf16 v[66:69], v[142:145], v[176:179], v[66:69]
	s_setprio 0
	s_barrier
	s_add_u32 s8, s8, 0x40080
	s_addc_u32 s9, s9, 0
	s_add_i32 s18, s18, s63
	s_mov_b32 m0, s18
	s_nop 0
	global_load_lds_dwordx4 v146, s[8:9]
	s_add_i32 m0, s18, 0x2000
	s_nop 0
	global_load_lds_dwordx4 v208, s[8:9]
	s_waitcnt vmcnt(6)
	s_mov_b32 s100, 0
	s_barrier
	s_setprio 1
	v_mfma_f32_16x16x32_bf16 v[30:33], v[180:183], v[148:151], v[30:33]
	v_mfma_f32_16x16x32_bf16 v[26:29], v[188:191], v[148:151], v[26:29]
	v_mfma_f32_16x16x32_bf16 v[22:25], v[180:183], v[156:159], v[22:25]
	v_mfma_f32_16x16x32_bf16 v[18:21], v[188:191], v[156:159], v[18:21]
	v_mfma_f32_16x16x32_bf16 v[14:17], v[180:183], v[164:167], v[14:17]
	v_mfma_f32_16x16x32_bf16 v[10:13], v[188:191], v[164:167], v[10:13]
	v_mfma_f32_16x16x32_bf16 v[6:9], v[180:183], v[172:175], v[6:9]
	v_mfma_f32_16x16x32_bf16 v[2:5], v[188:191], v[172:175], v[2:5]
	v_mfma_f32_16x16x32_bf16 v[30:33], v[184:187], v[152:155], v[30:33]
	v_mfma_f32_16x16x32_bf16 v[26:29], v[192:195], v[152:155], v[26:29]
	v_mfma_f32_16x16x32_bf16 v[22:25], v[184:187], v[160:163], v[22:25]
	v_mfma_f32_16x16x32_bf16 v[18:21], v[192:195], v[160:163], v[18:21]
	v_mfma_f32_16x16x32_bf16 v[14:17], v[184:187], v[168:171], v[14:17]
	v_mfma_f32_16x16x32_bf16 v[10:13], v[192:195], v[168:171], v[10:13]
	v_mfma_f32_16x16x32_bf16 v[6:9], v[184:187], v[176:179], v[6:9]
	v_mfma_f32_16x16x32_bf16 v[2:5], v[192:195], v[176:179], v[2:5]
	s_setprio 0
	s_add_i32 s7, s7, 2
	s_add_u32 s28, s28, 0x100
	s_addc_u32 s29, s29, 0
	s_add_u32 s1, s1, 0x100
	s_addc_u32 s2, s2, 0
	s_cmp_gt_u32 s7, 13
	s_barrier
	s_cbranch_scc1 .LBB0_256
